# MLA-prep row loop: the per-row s_waitcnt vmcnt(0) at the loop latch (it also waited for the row's six stores) relaxed to vmcnt(6) so only the next row's loads are awaited
# speedup vs baseline: 1.0019x; 1.0019x over previous
; __device__ __forceinline__ void ph_mla_prep(const Ptrs& P) {
;     ...
;     for (; u < R; u += G * 8) {
;         const int un = u + G * 8;
;         MlaRow nxt = cur;
;         if (un < R) nxt = mla_row_load(P, un, lane);
;     ...
;         cur = nxt;
;     }
.LBB0_991:
	s_or_b64 exec, exec, s[0:1]
	s_waitcnt vmcnt(6)
	v_mov_b64_e32 v[22:23], v[54:55]
	v_mov_b64_e32 v[26:27], v[50:51]
	v_mov_b64_e32 v[84:85], v[48:49]
	v_mov_b64_e32 v[80:81], v[44:45]
	v_mov_b64_e32 v[60:61], v[40:41]
	v_mov_b64_e32 v[100:101], v[20:21]
	v_mov_b64_e32 v[92:93], v[16:17]
	v_mov_b64_e32 v[88:89], v[32:33]
	v_mov_b64_e32 v[96:97], v[36:37]
	v_lshl_add_u64 v[110:111], v[110:111], 0, s[34:35]
	v_lshl_add_u64 v[114:115], v[114:115], 0, s[36:37]
	v_lshl_add_u64 v[118:119], v[118:119], 0, s[36:37]
	v_mov_b64_e32 v[24:25], v[56:57]
	v_mov_b64_e32 v[28:29], v[52:53]
	v_mov_b64_e32 v[82:83], v[46:47]
	v_mov_b64_e32 v[78:79], v[42:43]
	v_mov_b64_e32 v[58:59], v[38:39]
	v_mov_b64_e32 v[98:99], v[18:19]
	v_mov_b64_e32 v[90:91], v[14:15]
	v_mov_b64_e32 v[86:87], v[30:31]
	v_mov_b64_e32 v[94:95], v[34:35]
	v_mov_b32_e32 v116, v74
	v_mov_b32_e32 v6, v75
	v_mov_b32_e32 v112, v76
	v_mov_b32_e32 v8, v77
	v_mov_b32_e32 v128, v70
	v_mov_b32_e32 v10, v71
	v_mov_b32_e32 v126, v72
	v_mov_b32_e32 v12, v73
	v_mov_b32_e32 v117, v66
	v_mov_b32_e32 v7, v67
	v_mov_b32_e32 v113, v68
	v_mov_b32_e32 v9, v69
	v_mov_b32_e32 v129, v62
	v_mov_b32_e32 v11, v63
	v_mov_b32_e32 v127, v64
	v_mov_b32_e32 v13, v65
	s_andn2_b64 exec, exec, s[38:39]
	s_cbranch_execz .LBB0_1022
